# C2/C3 epilogues: fp8 converts write the store quads directly (no copies), dead zero-inits and dead address math removed
# speedup vs baseline: 1.0049x; 1.0049x over previous
; #define LAS __attribute__((address_space(3)))
; template <bool EMU> __device__ __forceinline__ float e2m3q(float y) { if constexpr (EMU) { y = fminf(fmaxf(y, -7.5f), 7.5f); return fabsf(y) < 1.f ? rintf(y * 8.f) * 0.125f : y; } else return y; }
;     static __device__ __forceinline__ f32x2 act2(f32x2 g, f32x2 l) {
;         g = __builtin_elementwise_min(g, (f32x2){7.f, 7.f}); l = __builtin_elementwise_min(__builtin_elementwise_max(l, (f32x2){-7.f, -7.f}), (f32x2){7.f, 7.f});
;         const f32x2 t = g * (-1.702f * 1.44269504089f); f32x2 e; e.x = __builtin_amdgcn_exp2f(t.x); e.y = __builtin_amdgcn_exp2f(t.y);
;         const f32x2 d = e + 1.0f; f32x2 r; r.x = __builtin_amdgcn_rcpf(d.x); r.y = __builtin_amdgcn_rcpf(d.y);
;         return (g * r) * (l * QS_ACT + QS_ACT);
;     __device__ __forceinline__ void operator()(const f32x4 (&acc)[2][2][4][2], const UnitD& u, int wr, int wc, int fr, int fq) const {
;         const int row0 = u.r0 + wr * 64 + fr, col0 = u.c0 + wc * 32 + 8 * fq;
;         const LAS float* bg = bl_lds + u.ui * 256 + wc * 32 + 8 * fq; const LAS float* bl = bg + 128;
;         f32x4 bgv[2], blv[2];
; #pragma unroll
;         for (int n = 0; n < 2; ++n) { bgv[n] = *(const LAS f32x4*)(bg + 4 * n); blv[n] = *(const LAS f32x4*)(bl + 4 * n); }
;         constexpr float SC = 1.f / (QS_X1 * QS_WUP);
; #pragma unroll
;         for (int ai = 0; ai < 2; ++ai)
; #pragma unroll
;             for (int m = 0; m < 4; ++m) { unsigned char* rowp = H + (size_t)(row0 + ai * 128 + m * 16) * DM + col0; u32x2 w;
; #pragma unroll
;                 for (int n = 0; n < 2; ++n) { const f32x4 g = acc[ai][0][m][n] * SC + bgv[n], l = acc[ai][1][m][n] * SC + blv[n];
;                     const f32x2 o0 = act2((f32x2){g[0], g[1]}, (f32x2){l[0], l[1]}), o1 = act2((f32x2){g[2], g[3]}, (f32x2){l[2], l[3]});
;                     int r = 0; r = __builtin_amdgcn_cvt_pk_fp8_f32(e2m3q<EMU_DOWN != 0>(o0.x), e2m3q<EMU_DOWN != 0>(o0.y), r, false); r = __builtin_amdgcn_cvt_pk_fp8_f32(e2m3q<EMU_DOWN != 0>(o1.x), e2m3q<EMU_DOWN != 0>(o1.y), r, true);
;                     if (n == 0) w.x = (unsigned)r; else w.y = (unsigned)r; }
;                 *(u32x2*)rowp = w; }
.LBB0_755:
	s_add_u32 s18, s85, 0xffffff00
	v_mov_b32_e32 v16, v154
	v_bfe_u32 v152, v154, 4, 1
	s_addc_u32 s19, s86, -1
	s_lshl_b32 s20, s76, 10
	v_mul_u32_u24_e32 v152, 0x3ff8, v152
	v_lshrrev_b32_e32 v0, 1, v16
	v_and_b32_e32 v18, 0x60, v0
	v_and_b32_e32 v19, 24, v0
	s_add_i32 s20, s20, 0
	s_add_i32 s20, s20, 0x23100
	v_lshlrev_b32_e32 v0, 2, v18
	v_lshlrev_b32_e32 v1, 2, v19
	v_add3_u32 v4, s20, v0, v1
	ds_read_b128 v[8:11], v4
	ds_read_b128 v[0:3], v4 offset:16
	ds_read_b128 v[12:15], v4 offset:512
	ds_read_b128 v[4:7], v4 offset:528
	v_and_b32_e32 v17, 15, v16
	s_waitcnt lgkmcnt(0)
	v_pk_fma_f32 v[22:23], v[148:149], s[36:37], v[8:9] op_sel_hi:[1,0,1]
	v_ashrrev_i32_e32 v20, 2, v16
	v_min_f32_e32 v23, 0x40e00000, v23
	v_min_f32_e32 v22, 0x40e00000, v22
	v_pk_mul_f32 v[176:177], v[22:23], s[78:79] op_sel_hi:[1,0]
	v_pk_fma_f32 v[174:175], v[116:117], s[36:37], v[12:13] op_sel_hi:[1,0,1]
	v_exp_f32_e32 v176, v176
	v_exp_f32_e32 v177, v177
	v_and_or_b32 v17, v20, s39, v17
	v_pk_fma_f32 v[20:21], v[150:151], s[36:37], v[10:11] op_sel_hi:[1,0,1]
	v_med3_f32 v175, v175, s47, v190
	v_pk_add_f32 v[176:177], v[176:177], 1.0 op_sel_hi:[1,0]
	v_med3_f32 v174, v174, s47, v190
	v_rcp_f32_e32 v176, v176
	v_rcp_f32_e32 v177, v177
	v_pk_fma_f32 v[174:175], v[174:175], 4.0, 4.0 op_sel_hi:[1,0,0]
	v_min_f32_e32 v21, 0x40e00000, v21
	v_min_f32_e32 v20, 0x40e00000, v20
	v_pk_mul_f32 v[22:23], v[22:23], v[176:177]
	v_pk_fma_f32 v[172:173], v[118:119], s[36:37], v[14:15] op_sel_hi:[1,0,1]
	v_pk_mul_f32 v[22:23], v[174:175], v[22:23]
	v_pk_mul_f32 v[174:175], v[20:21], s[78:79] op_sel_hi:[1,0]
	v_med3_f32 v173, v173, s47, v190
	v_exp_f32_e32 v174, v174
	v_exp_f32_e32 v175, v175
	v_med3_f32 v172, v172, s47, v190
	v_pk_fma_f32 v[172:173], v[172:173], 4.0, 4.0 op_sel_hi:[1,0,0]
	v_pk_fma_f32 v[176:177], v[112:113], s[36:37], v[4:5] op_sel_hi:[1,0,1]
	v_pk_add_f32 v[174:175], v[174:175], 1.0 op_sel_hi:[1,0]
	v_med3_f32 v177, v177, s47, v190
	v_rcp_f32_e32 v174, v174
	v_rcp_f32_e32 v175, v175
	v_med3_f32 v176, v176, s47, v190
	v_pk_fma_f32 v[176:177], v[176:177], 4.0, 4.0 op_sel_hi:[1,0,0]
	v_add3_u32 v16, v18, s2, v19
	v_pk_mul_f32 v[20:21], v[20:21], v[174:175]
	v_pk_fma_f32 v[174:175], v[114:115], s[36:37], v[6:7] op_sel_hi:[1,0,1]
	v_pk_mul_f32 v[20:21], v[172:173], v[20:21]
	v_cvt_pk_fp8_f32 v148, v22, v23
	v_pk_fma_f32 v[22:23], v[144:145], s[36:37], v[0:1] op_sel_hi:[1,0,1]
	v_min_f32_e32 v23, 0x40e00000, v23
	v_min_f32_e32 v22, 0x40e00000, v22
	v_pk_mul_f32 v[178:179], v[22:23], s[78:79] op_sel_hi:[1,0]
	v_cvt_pk_fp8_f32 v148, v20, v21 op_sel:[0,0,1]
	v_exp_f32_e32 v178, v178
	v_exp_f32_e32 v179, v179
	v_pk_fma_f32 v[20:21], v[146:147], s[36:37], v[2:3] op_sel_hi:[1,0,1]
	v_med3_f32 v175, v175, s47, v190
	v_min_f32_e32 v21, 0x40e00000, v21
	v_pk_add_f32 v[178:179], v[178:179], 1.0 op_sel_hi:[1,0]
	v_min_f32_e32 v20, 0x40e00000, v20
	v_rcp_f32_e32 v178, v178
	v_rcp_f32_e32 v179, v179
	v_med3_f32 v174, v174, s47, v190
	v_pk_fma_f32 v[174:175], v[174:175], 4.0, 4.0 op_sel_hi:[1,0,0]
	v_add_u32_e32 v18, s68, v17
	v_pk_mul_f32 v[22:23], v[22:23], v[178:179]
	v_ashrrev_i32_e32 v19, 31, v18
	v_pk_mul_f32 v[22:23], v[176:177], v[22:23]
	v_pk_mul_f32 v[176:177], v[20:21], s[78:79] op_sel_hi:[1,0]
	v_cvt_pk_fp8_f32 v149, v22, v23
	v_exp_f32_e32 v176, v176
	v_exp_f32_e32 v177, v177
	v_lshlrev_b64 v[18:19], 10, v[18:19]
	v_ashrrev_i32_e32 v17, 31, v16
	v_lshl_add_u64 v[18:19], s[6:7], 0, v[18:19]
	v_pk_add_f32 v[176:177], v[176:177], 1.0 op_sel_hi:[1,0]
	v_lshl_add_u64 v[16:17], v[18:19], 0, v[16:17]
	s_nop 0
	v_lshl_add_u64 v[144:145], v[16:17], 0, v[152:153]
	v_rcp_f32_e32 v176, v176
	v_rcp_f32_e32 v177, v177
	v_pk_fma_f32 v[18:19], v[142:143], s[36:37], v[10:11] op_sel_hi:[1,0,1]
	v_pk_fma_f32 v[22:23], v[110:111], s[36:37], v[14:15] op_sel_hi:[1,0,1]
	v_min_f32_e32 v19, 0x40e00000, v19
	v_pk_mul_f32 v[20:21], v[20:21], v[176:177]
	v_min_f32_e32 v18, 0x40e00000, v18
	v_pk_mul_f32 v[20:21], v[174:175], v[20:21]
	v_med3_f32 v23, v23, s47, v190
	v_cvt_pk_fp8_f32 v149, v20, v21 op_sel:[0,0,1]
	v_pk_fma_f32 v[20:21], v[140:141], s[36:37], v[8:9] op_sel_hi:[1,0,1]
	v_med3_f32 v22, v22, s47, v190
	v_min_f32_e32 v21, 0x40e00000, v21
	v_min_f32_e32 v20, 0x40e00000, v20
	v_pk_mul_f32 v[174:175], v[20:21], s[78:79] op_sel_hi:[1,0]
	v_exp_f32_e32 v174, v174
	v_exp_f32_e32 v175, v175
	v_pk_fma_f32 v[172:173], v[108:109], s[36:37], v[12:13] op_sel_hi:[1,0,1]
	v_pk_fma_f32 v[22:23], v[22:23], 4.0, 4.0 op_sel_hi:[1,0,0]
	v_med3_f32 v173, v173, s47, v190
	v_pk_add_f32 v[174:175], v[174:175], 1.0 op_sel_hi:[1,0]
	v_med3_f32 v172, v172, s47, v190
	v_rcp_f32_e32 v174, v174
	v_rcp_f32_e32 v175, v175
	v_pk_fma_f32 v[172:173], v[172:173], 4.0, 4.0 op_sel_hi:[1,0,0]
	s_movk_i32 s20, 0x4000
	s_mov_b64 s[88:89], 0x42040080
	v_pk_mul_f32 v[20:21], v[20:21], v[174:175]
	v_pk_fma_f32 v[174:175], v[104:105], s[36:37], v[4:5] op_sel_hi:[1,0,1]
	v_pk_mul_f32 v[20:21], v[172:173], v[20:21]
	v_pk_mul_f32 v[172:173], v[18:19], s[78:79] op_sel_hi:[1,0]
	v_med3_f32 v175, v175, s47, v190
	v_exp_f32_e32 v172, v172
	v_exp_f32_e32 v173, v173
	v_med3_f32 v174, v174, s47, v190
	v_pk_fma_f32 v[174:175], v[174:175], 4.0, 4.0 op_sel_hi:[1,0,0]
	v_pk_add_f32 v[172:173], v[172:173], 1.0 op_sel_hi:[1,0]
	s_nop 0
	v_rcp_f32_e32 v172, v172
	v_rcp_f32_e32 v173, v173
	s_nop 0
	v_pk_mul_f32 v[18:19], v[18:19], v[172:173]
	s_nop 0
	v_pk_mul_f32 v[18:19], v[22:23], v[18:19]
	v_cvt_pk_fp8_f32 v150, v20, v21
	v_pk_fma_f32 v[20:21], v[136:137], s[36:37], v[0:1] op_sel_hi:[1,0,1]
	v_min_f32_e32 v21, 0x40e00000, v21
	v_min_f32_e32 v20, 0x40e00000, v20
	v_pk_mul_f32 v[176:177], v[20:21], s[78:79] op_sel_hi:[1,0]
; #define LAS __attribute__((address_space(3)))
; template <bool EMU> __device__ __forceinline__ float e2m3q(float y) { if constexpr (EMU) { y = fminf(fmaxf(y, -7.5f), 7.5f); return fabsf(y) < 1.f ? rintf(y * 8.f) * 0.125f : y; } else return y; }
;     static __device__ __forceinline__ f32x2 act2(f32x2 g, f32x2 l) {
;         g = __builtin_elementwise_min(g, (f32x2){7.f, 7.f}); l = __builtin_elementwise_min(__builtin_elementwise_max(l, (f32x2){-7.f, -7.f}), (f32x2){7.f, 7.f});
;         const f32x2 t = g * (-1.702f * 1.44269504089f); f32x2 e; e.x = __builtin_amdgcn_exp2f(t.x); e.y = __builtin_amdgcn_exp2f(t.y);
;         const f32x2 d = e + 1.0f; f32x2 r; r.x = __builtin_amdgcn_rcpf(d.x); r.y = __builtin_amdgcn_rcpf(d.y);
;         return (g * r) * (l * QS_ACT + QS_ACT);
;     __device__ __forceinline__ void operator()(const f32x4 (&acc)[2][2][4][2], const UnitD& u, int wr, int wc, int fr, int fq) const {
;         const int row0 = u.r0 + wr * 64 + fr, col0 = u.c0 + wc * 32 + 8 * fq;
;         const LAS float* bg = bl_lds + u.ui * 256 + wc * 32 + 8 * fq; const LAS float* bl = bg + 128;
;         f32x4 bgv[2], blv[2];
; #pragma unroll
;         for (int n = 0; n < 2; ++n) { bgv[n] = *(const LAS f32x4*)(bg + 4 * n); blv[n] = *(const LAS f32x4*)(bl + 4 * n); }
;         constexpr float SC = 1.f / (QS_X1 * QS_WUP);
; #pragma unroll
;         for (int ai = 0; ai < 2; ++ai)
; #pragma unroll
;             for (int m = 0; m < 4; ++m) { unsigned char* rowp = H + (size_t)(row0 + ai * 128 + m * 16) * DM + col0; u32x2 w;
; #pragma unroll
;                 for (int n = 0; n < 2; ++n) { const f32x4 g = acc[ai][0][m][n] * SC + bgv[n], l = acc[ai][1][m][n] * SC + blv[n];
;                     const f32x2 o0 = act2((f32x2){g[0], g[1]}, (f32x2){l[0], l[1]}), o1 = act2((f32x2){g[2], g[3]}, (f32x2){l[2], l[3]});
;                     int r = 0; r = __builtin_amdgcn_cvt_pk_fp8_f32(e2m3q<EMU_DOWN != 0>(o0.x), e2m3q<EMU_DOWN != 0>(o0.y), r, false); r = __builtin_amdgcn_cvt_pk_fp8_f32(e2m3q<EMU_DOWN != 0>(o1.x), e2m3q<EMU_DOWN != 0>(o1.y), r, true);
;                     if (n == 0) w.x = (unsigned)r; else w.y = (unsigned)r; }
;                 *(u32x2*)rowp = w; }
	v_cvt_pk_fp8_f32 v150, v18, v19 op_sel:[0,0,1]
	v_exp_f32_e32 v176, v176
	v_exp_f32_e32 v177, v177
	v_pk_fma_f32 v[18:19], v[138:139], s[36:37], v[2:3] op_sel_hi:[1,0,1]
	v_pk_fma_f32 v[172:173], v[106:107], s[36:37], v[6:7] op_sel_hi:[1,0,1]
	v_min_f32_e32 v19, 0x40e00000, v19
	v_pk_add_f32 v[176:177], v[176:177], 1.0 op_sel_hi:[1,0]
	v_min_f32_e32 v18, 0x40e00000, v18
	v_rcp_f32_e32 v176, v176
	v_rcp_f32_e32 v177, v177
	v_med3_f32 v173, v173, s47, v190
	v_med3_f32 v172, v172, s47, v190
	v_pk_fma_f32 v[172:173], v[172:173], 4.0, 4.0 op_sel_hi:[1,0,0]
	v_pk_mul_f32 v[20:21], v[20:21], v[176:177]
	s_nop 0
	v_pk_mul_f32 v[20:21], v[174:175], v[20:21]
	v_pk_mul_f32 v[174:175], v[18:19], s[78:79] op_sel_hi:[1,0]
	v_cvt_pk_fp8_f32 v151, v20, v21
	v_exp_f32_e32 v174, v174
	v_exp_f32_e32 v175, v175
	v_pk_fma_f32 v[20:21], v[132:133], s[36:37], v[8:9] op_sel_hi:[1,0,1]
	v_pk_add_f32 v[174:175], v[174:175], 1.0 op_sel_hi:[1,0]
	s_nop 0
	v_rcp_f32_e32 v174, v174
	v_rcp_f32_e32 v175, v175
	v_min_f32_e32 v21, 0x40e00000, v21
	v_min_f32_e32 v20, 0x40e00000, v20
	v_pk_mul_f32 v[18:19], v[18:19], v[174:175]
	v_pk_mul_f32 v[174:175], v[20:21], s[78:79] op_sel_hi:[1,0]
	v_pk_mul_f32 v[18:19], v[172:173], v[18:19]
	v_exp_f32_e32 v174, v174
	v_exp_f32_e32 v175, v175
	v_cvt_pk_fp8_f32 v151, v18, v19 op_sel:[0,0,1]
	v_add_co_u32_e32 v18, vcc, s20, v16
	v_pk_add_f32 v[174:175], v[174:175], 1.0 op_sel_hi:[1,0]
	s_nop 0
	v_addc_co_u32_e32 v19, vcc, 0, v17, vcc
	v_rcp_f32_e32 v174, v174
	v_rcp_f32_e32 v175, v175
	v_pk_fma_f32 v[172:173], v[100:101], s[36:37], v[12:13] op_sel_hi:[1,0,1]
	v_permlane16_swap_b32_e32 v148, v150
	v_permlane16_swap_b32_e32 v149, v151
	global_store_dwordx4 v[144:145], v[148:151], off
	v_pk_fma_f32 v[18:19], v[134:135], s[36:37], v[10:11] op_sel_hi:[1,0,1]
	v_med3_f32 v173, v173, s47, v190
	v_med3_f32 v172, v172, s47, v190
	v_pk_mul_f32 v[20:21], v[20:21], v[174:175]
	v_pk_fma_f32 v[172:173], v[172:173], 4.0, 4.0 op_sel_hi:[1,0,0]
	v_min_f32_e32 v19, 0x40e00000, v19
	v_min_f32_e32 v18, 0x40e00000, v18
	v_pk_mul_f32 v[20:21], v[172:173], v[20:21]
	v_pk_mul_f32 v[172:173], v[18:19], s[78:79] op_sel_hi:[1,0]
	v_pk_fma_f32 v[22:23], v[102:103], s[36:37], v[14:15] op_sel_hi:[1,0,1]
	v_exp_f32_e32 v172, v172
	v_exp_f32_e32 v173, v173
	v_med3_f32 v23, v23, s47, v190
	v_med3_f32 v22, v22, s47, v190
	v_pk_fma_f32 v[22:23], v[22:23], 4.0, 4.0 op_sel_hi:[1,0,0]
	v_pk_add_f32 v[172:173], v[172:173], 1.0 op_sel_hi:[1,0]
	v_pk_fma_f32 v[174:175], v[96:97], s[36:37], v[4:5] op_sel_hi:[1,0,1]
	v_rcp_f32_e32 v172, v172
	v_rcp_f32_e32 v173, v173
	v_med3_f32 v175, v175, s47, v190
	v_med3_f32 v174, v174, s47, v190
	v_pk_fma_f32 v[174:175], v[174:175], 4.0, 4.0 op_sel_hi:[1,0,0]
	v_pk_mul_f32 v[18:19], v[18:19], v[172:173]
	v_pk_fma_f32 v[172:173], v[98:99], s[36:37], v[6:7] op_sel_hi:[1,0,1]
	v_pk_mul_f32 v[18:19], v[22:23], v[18:19]
	v_cvt_pk_fp8_f32 v148, v20, v21
	v_pk_fma_f32 v[20:21], v[128:129], s[36:37], v[0:1] op_sel_hi:[1,0,1]
	v_min_f32_e32 v21, 0x40e00000, v21
	v_min_f32_e32 v20, 0x40e00000, v20
	v_pk_mul_f32 v[176:177], v[20:21], s[78:79] op_sel_hi:[1,0]
	v_cvt_pk_fp8_f32 v148, v18, v19 op_sel:[0,0,1]
	v_exp_f32_e32 v176, v176
	v_exp_f32_e32 v177, v177
	v_pk_fma_f32 v[18:19], v[130:131], s[36:37], v[2:3] op_sel_hi:[1,0,1]
	v_med3_f32 v173, v173, s47, v190
	v_min_f32_e32 v19, 0x40e00000, v19
	v_pk_add_f32 v[176:177], v[176:177], 1.0 op_sel_hi:[1,0]
	v_min_f32_e32 v18, 0x40e00000, v18
	v_rcp_f32_e32 v176, v176
	v_rcp_f32_e32 v177, v177
	v_med3_f32 v172, v172, s47, v190
	v_pk_fma_f32 v[172:173], v[172:173], 4.0, 4.0 op_sel_hi:[1,0,0]
	s_mov_b32 s20, 0x8000
	v_pk_mul_f32 v[20:21], v[20:21], v[176:177]
	s_nop 0
	v_pk_mul_f32 v[20:21], v[174:175], v[20:21]
	v_pk_mul_f32 v[174:175], v[18:19], s[78:79] op_sel_hi:[1,0]
	v_cvt_pk_fp8_f32 v149, v20, v21
	v_exp_f32_e32 v174, v174
	v_exp_f32_e32 v175, v175
	v_pk_fma_f32 v[20:21], v[124:125], s[36:37], v[8:9] op_sel_hi:[1,0,1]
	v_pk_add_f32 v[174:175], v[174:175], 1.0 op_sel_hi:[1,0]
	s_nop 0
	v_rcp_f32_e32 v174, v174
	v_rcp_f32_e32 v175, v175
	v_min_f32_e32 v21, 0x40e00000, v21
	v_min_f32_e32 v20, 0x40e00000, v20
	v_pk_mul_f32 v[18:19], v[18:19], v[174:175]
	v_pk_mul_f32 v[174:175], v[20:21], s[78:79] op_sel_hi:[1,0]
	v_pk_mul_f32 v[18:19], v[172:173], v[18:19]
	v_exp_f32_e32 v174, v174
	v_exp_f32_e32 v175, v175
	v_cvt_pk_fp8_f32 v149, v18, v19 op_sel:[0,0,1]
	v_add_co_u32_e32 v18, vcc, s20, v16
	v_pk_add_f32 v[174:175], v[174:175], 1.0 op_sel_hi:[1,0]
	s_nop 0
	v_addc_co_u32_e32 v19, vcc, 0, v17, vcc
	v_rcp_f32_e32 v174, v174
	v_rcp_f32_e32 v175, v175
	v_pk_fma_f32 v[172:173], v[92:93], s[36:37], v[12:13] op_sel_hi:[1,0,1]
	v_lshl_add_u64 v[146:147], v[18:19], 0, v[152:153]
	v_pk_fma_f32 v[18:19], v[126:127], s[36:37], v[10:11] op_sel_hi:[1,0,1]
	v_med3_f32 v173, v173, s47, v190
	v_med3_f32 v172, v172, s47, v190
	v_pk_mul_f32 v[20:21], v[20:21], v[174:175]
	v_pk_fma_f32 v[172:173], v[172:173], 4.0, 4.0 op_sel_hi:[1,0,0]
	v_min_f32_e32 v19, 0x40e00000, v19
	v_min_f32_e32 v18, 0x40e00000, v18
	v_pk_mul_f32 v[20:21], v[172:173], v[20:21]
	v_pk_mul_f32 v[172:173], v[18:19], s[78:79] op_sel_hi:[1,0]
	v_pk_fma_f32 v[22:23], v[94:95], s[36:37], v[14:15] op_sel_hi:[1,0,1]
	v_exp_f32_e32 v172, v172
	v_exp_f32_e32 v173, v173
	v_med3_f32 v23, v23, s47, v190
	v_med3_f32 v22, v22, s47, v190
	v_pk_fma_f32 v[22:23], v[22:23], 4.0, 4.0 op_sel_hi:[1,0,0]
	v_pk_add_f32 v[172:173], v[172:173], 1.0 op_sel_hi:[1,0]
	v_pk_fma_f32 v[174:175], v[88:89], s[36:37], v[4:5] op_sel_hi:[1,0,1]
	v_rcp_f32_e32 v172, v172
	v_rcp_f32_e32 v173, v173
	v_med3_f32 v175, v175, s47, v190
	v_med3_f32 v174, v174, s47, v190
; #define LAS __attribute__((address_space(3)))
; template <bool EMU> __device__ __forceinline__ float e2m3q(float y) { if constexpr (EMU) { y = fminf(fmaxf(y, -7.5f), 7.5f); return fabsf(y) < 1.f ? rintf(y * 8.f) * 0.125f : y; } else return y; }
;     static __device__ __forceinline__ f32x2 act2(f32x2 g, f32x2 l) {
;         g = __builtin_elementwise_min(g, (f32x2){7.f, 7.f}); l = __builtin_elementwise_min(__builtin_elementwise_max(l, (f32x2){-7.f, -7.f}), (f32x2){7.f, 7.f});
;         const f32x2 t = g * (-1.702f * 1.44269504089f); f32x2 e; e.x = __builtin_amdgcn_exp2f(t.x); e.y = __builtin_amdgcn_exp2f(t.y);
;         const f32x2 d = e + 1.0f; f32x2 r; r.x = __builtin_amdgcn_rcpf(d.x); r.y = __builtin_amdgcn_rcpf(d.y);
;         return (g * r) * (l * QS_ACT + QS_ACT);
;     }
;     __device__ __forceinline__ void operator()(const f32x4 (&acc)[2][2][4][2], const UnitD& u, int wr, int wc, int fr, int fq) const {
;         const int row0 = u.r0 + wr * 64 + fr, col0 = u.c0 + wc * 32 + 8 * fq;
;         const LAS float* bg = bl_lds + u.ui * 256 + wc * 32 + 8 * fq; const LAS float* bl = bg + 128;
;         f32x4 bgv[2], blv[2];
; #pragma unroll
;         for (int n = 0; n < 2; ++n) { bgv[n] = *(const LAS f32x4*)(bg + 4 * n); blv[n] = *(const LAS f32x4*)(bl + 4 * n); }
;         constexpr float SC = 1.f / (QS_X1 * QS_WUP);
; #pragma unroll
;         for (int ai = 0; ai < 2; ++ai)
; #pragma unroll
;             for (int m = 0; m < 4; ++m) { unsigned char* rowp = H + (size_t)(row0 + ai * 128 + m * 16) * DM + col0; u32x2 w;
; #pragma unroll
;                 for (int n = 0; n < 2; ++n) { const f32x4 g = acc[ai][0][m][n] * SC + bgv[n], l = acc[ai][1][m][n] * SC + blv[n];
;                     const f32x2 o0 = act2((f32x2){g[0], g[1]}, (f32x2){l[0], l[1]}), o1 = act2((f32x2){g[2], g[3]}, (f32x2){l[2], l[3]});
;                     int r = 0; r = __builtin_amdgcn_cvt_pk_fp8_f32(e2m3q<EMU_DOWN != 0>(o0.x), e2m3q<EMU_DOWN != 0>(o0.y), r, false); r = __builtin_amdgcn_cvt_pk_fp8_f32(e2m3q<EMU_DOWN != 0>(o1.x), e2m3q<EMU_DOWN != 0>(o1.y), r, true);
;                     if (n == 0) w.x = (unsigned)r; else w.y = (unsigned)r; }
;                 *(u32x2*)rowp = w; }
	v_pk_fma_f32 v[174:175], v[174:175], 4.0, 4.0 op_sel_hi:[1,0,0]
	v_pk_mul_f32 v[18:19], v[18:19], v[172:173]
	v_pk_fma_f32 v[172:173], v[90:91], s[36:37], v[6:7] op_sel_hi:[1,0,1]
	v_pk_mul_f32 v[18:19], v[22:23], v[18:19]
	v_cvt_pk_fp8_f32 v150, v20, v21
	v_pk_fma_f32 v[20:21], v[120:121], s[36:37], v[0:1] op_sel_hi:[1,0,1]
	v_min_f32_e32 v21, 0x40e00000, v21
	v_min_f32_e32 v20, 0x40e00000, v20
	v_pk_mul_f32 v[176:177], v[20:21], s[78:79] op_sel_hi:[1,0]
	v_cvt_pk_fp8_f32 v150, v18, v19 op_sel:[0,0,1]
	v_exp_f32_e32 v176, v176
	v_exp_f32_e32 v177, v177
	v_pk_fma_f32 v[18:19], v[122:123], s[36:37], v[2:3] op_sel_hi:[1,0,1]
	v_med3_f32 v173, v173, s47, v190
	v_min_f32_e32 v19, 0x40e00000, v19
	v_pk_add_f32 v[176:177], v[176:177], 1.0 op_sel_hi:[1,0]
	v_min_f32_e32 v18, 0x40e00000, v18
	v_rcp_f32_e32 v176, v176
	v_rcp_f32_e32 v177, v177
	v_med3_f32 v172, v172, s47, v190
	v_pk_fma_f32 v[172:173], v[172:173], 4.0, 4.0 op_sel_hi:[1,0,0]
	s_mov_b32 s20, 0xc000
	v_pk_mul_f32 v[20:21], v[20:21], v[176:177]
	s_nop 0
	v_pk_mul_f32 v[20:21], v[174:175], v[20:21]
	v_pk_mul_f32 v[174:175], v[18:19], s[78:79] op_sel_hi:[1,0]
	v_cvt_pk_fp8_f32 v151, v20, v21
	v_exp_f32_e32 v174, v174
	v_exp_f32_e32 v175, v175
	v_pk_fma_f32 v[20:21], v[84:85], s[36:37], v[8:9] op_sel_hi:[1,0,1]
	v_pk_add_f32 v[174:175], v[174:175], 1.0 op_sel_hi:[1,0]
	s_nop 0
	v_rcp_f32_e32 v174, v174
	v_rcp_f32_e32 v175, v175
	v_min_f32_e32 v21, 0x40e00000, v21
	v_min_f32_e32 v20, 0x40e00000, v20
	v_pk_mul_f32 v[18:19], v[18:19], v[174:175]
	v_pk_mul_f32 v[174:175], v[20:21], s[78:79] op_sel_hi:[1,0]
	v_pk_mul_f32 v[18:19], v[172:173], v[18:19]
	v_exp_f32_e32 v174, v174
	v_exp_f32_e32 v175, v175
	v_cvt_pk_fp8_f32 v151, v18, v19 op_sel:[0,0,1]
	v_add_co_u32_e32 v18, vcc, s20, v16
	v_pk_add_f32 v[174:175], v[174:175], 1.0 op_sel_hi:[1,0]
	s_nop 0
	v_addc_co_u32_e32 v19, vcc, 0, v17, vcc
	v_rcp_f32_e32 v174, v174
	v_rcp_f32_e32 v175, v175
	v_pk_fma_f32 v[172:173], v[52:53], s[36:37], v[12:13] op_sel_hi:[1,0,1]
	v_permlane16_swap_b32_e32 v148, v150
	v_permlane16_swap_b32_e32 v149, v151
	global_store_dwordx4 v[146:147], v[148:151], off
	v_pk_fma_f32 v[18:19], v[86:87], s[36:37], v[10:11] op_sel_hi:[1,0,1]
	v_med3_f32 v173, v173, s47, v190
	v_med3_f32 v172, v172, s47, v190
	v_pk_mul_f32 v[20:21], v[20:21], v[174:175]
	v_pk_fma_f32 v[172:173], v[172:173], 4.0, 4.0 op_sel_hi:[1,0,0]
	v_min_f32_e32 v19, 0x40e00000, v19
	v_min_f32_e32 v18, 0x40e00000, v18
	v_pk_mul_f32 v[20:21], v[172:173], v[20:21]
	v_pk_mul_f32 v[172:173], v[18:19], s[78:79] op_sel_hi:[1,0]
	v_pk_fma_f32 v[22:23], v[54:55], s[36:37], v[14:15] op_sel_hi:[1,0,1]
	v_exp_f32_e32 v172, v172
	v_exp_f32_e32 v173, v173
	v_med3_f32 v23, v23, s47, v190
	v_med3_f32 v22, v22, s47, v190
	v_pk_fma_f32 v[22:23], v[22:23], 4.0, 4.0 op_sel_hi:[1,0,0]
	v_pk_add_f32 v[172:173], v[172:173], 1.0 op_sel_hi:[1,0]
	v_pk_fma_f32 v[174:175], v[48:49], s[36:37], v[4:5] op_sel_hi:[1,0,1]
	v_rcp_f32_e32 v172, v172
	v_rcp_f32_e32 v173, v173
	v_med3_f32 v175, v175, s47, v190
	v_med3_f32 v174, v174, s47, v190
	v_pk_fma_f32 v[174:175], v[174:175], 4.0, 4.0 op_sel_hi:[1,0,0]
	v_pk_mul_f32 v[18:19], v[18:19], v[172:173]
	v_pk_fma_f32 v[172:173], v[50:51], s[36:37], v[6:7] op_sel_hi:[1,0,1]
	v_pk_mul_f32 v[18:19], v[22:23], v[18:19]
	v_cvt_pk_fp8_f32 v148, v20, v21
	v_pk_fma_f32 v[20:21], v[80:81], s[36:37], v[0:1] op_sel_hi:[1,0,1]
	v_min_f32_e32 v21, 0x40e00000, v21
	v_min_f32_e32 v20, 0x40e00000, v20
	v_pk_mul_f32 v[176:177], v[20:21], s[78:79] op_sel_hi:[1,0]
	v_cvt_pk_fp8_f32 v148, v18, v19 op_sel:[0,0,1]
	v_exp_f32_e32 v176, v176
	v_exp_f32_e32 v177, v177
	v_pk_fma_f32 v[18:19], v[82:83], s[36:37], v[2:3] op_sel_hi:[1,0,1]
	v_med3_f32 v173, v173, s47, v190
	v_min_f32_e32 v19, 0x40e00000, v19
	v_pk_add_f32 v[176:177], v[176:177], 1.0 op_sel_hi:[1,0]
	v_min_f32_e32 v18, 0x40e00000, v18
	v_rcp_f32_e32 v176, v176
	v_rcp_f32_e32 v177, v177
	v_med3_f32 v172, v172, s47, v190
	v_pk_fma_f32 v[172:173], v[172:173], 4.0, 4.0 op_sel_hi:[1,0,0]
	s_mov_b32 s20, 0x20000
	v_pk_mul_f32 v[20:21], v[20:21], v[176:177]
	s_nop 0
	v_pk_mul_f32 v[20:21], v[174:175], v[20:21]
	v_pk_mul_f32 v[174:175], v[18:19], s[78:79] op_sel_hi:[1,0]
	v_cvt_pk_fp8_f32 v149, v20, v21
	v_exp_f32_e32 v174, v174
	v_exp_f32_e32 v175, v175
	v_pk_fma_f32 v[20:21], v[76:77], s[36:37], v[8:9] op_sel_hi:[1,0,1]
	v_pk_add_f32 v[174:175], v[174:175], 1.0 op_sel_hi:[1,0]
	s_nop 0
	v_rcp_f32_e32 v174, v174
	v_rcp_f32_e32 v175, v175
	v_min_f32_e32 v21, 0x40e00000, v21
	v_min_f32_e32 v20, 0x40e00000, v20
	v_pk_mul_f32 v[18:19], v[18:19], v[174:175]
	v_pk_mul_f32 v[174:175], v[20:21], s[78:79] op_sel_hi:[1,0]
	v_pk_mul_f32 v[18:19], v[172:173], v[18:19]
	v_exp_f32_e32 v174, v174
	v_exp_f32_e32 v175, v175
	v_cvt_pk_fp8_f32 v149, v18, v19 op_sel:[0,0,1]
	v_add_co_u32_e32 v18, vcc, s20, v16
	v_pk_add_f32 v[174:175], v[174:175], 1.0 op_sel_hi:[1,0]
	s_nop 0
	v_addc_co_u32_e32 v19, vcc, 0, v17, vcc
	v_rcp_f32_e32 v174, v174
	v_rcp_f32_e32 v175, v175
	v_pk_fma_f32 v[172:173], v[44:45], s[36:37], v[12:13] op_sel_hi:[1,0,1]
	v_lshl_add_u64 v[146:147], v[18:19], 0, v[152:153]
	v_pk_fma_f32 v[18:19], v[78:79], s[36:37], v[10:11] op_sel_hi:[1,0,1]
	v_med3_f32 v173, v173, s47, v190
	v_med3_f32 v172, v172, s47, v190
	v_pk_mul_f32 v[20:21], v[20:21], v[174:175]
	v_pk_fma_f32 v[172:173], v[172:173], 4.0, 4.0 op_sel_hi:[1,0,0]
	v_min_f32_e32 v19, 0x40e00000, v19
	v_min_f32_e32 v18, 0x40e00000, v18
	v_pk_mul_f32 v[20:21], v[172:173], v[20:21]
	v_pk_mul_f32 v[172:173], v[18:19], s[78:79] op_sel_hi:[1,0]
	v_pk_fma_f32 v[22:23], v[46:47], s[36:37], v[14:15] op_sel_hi:[1,0,1]
	v_exp_f32_e32 v172, v172
	v_exp_f32_e32 v173, v173
; #define LAS __attribute__((address_space(3)))
; template <bool EMU> __device__ __forceinline__ float e2m3q(float y) { if constexpr (EMU) { y = fminf(fmaxf(y, -7.5f), 7.5f); return fabsf(y) < 1.f ? rintf(y * 8.f) * 0.125f : y; } else return y; }
;     static __device__ __forceinline__ f32x2 act2(f32x2 g, f32x2 l) {
;         g = __builtin_elementwise_min(g, (f32x2){7.f, 7.f}); l = __builtin_elementwise_min(__builtin_elementwise_max(l, (f32x2){-7.f, -7.f}), (f32x2){7.f, 7.f});
;         const f32x2 t = g * (-1.702f * 1.44269504089f); f32x2 e; e.x = __builtin_amdgcn_exp2f(t.x); e.y = __builtin_amdgcn_exp2f(t.y);
;         const f32x2 d = e + 1.0f; f32x2 r; r.x = __builtin_amdgcn_rcpf(d.x); r.y = __builtin_amdgcn_rcpf(d.y);
;         return (g * r) * (l * QS_ACT + QS_ACT);
;     }
;     __device__ __forceinline__ void operator()(const f32x4 (&acc)[2][2][4][2], const UnitD& u, int wr, int wc, int fr, int fq) const {
;         const int row0 = u.r0 + wr * 64 + fr, col0 = u.c0 + wc * 32 + 8 * fq;
;         const LAS float* bg = bl_lds + u.ui * 256 + wc * 32 + 8 * fq; const LAS float* bl = bg + 128;
;         f32x4 bgv[2], blv[2];
; #pragma unroll
;         for (int n = 0; n < 2; ++n) { bgv[n] = *(const LAS f32x4*)(bg + 4 * n); blv[n] = *(const LAS f32x4*)(bl + 4 * n); }
;         constexpr float SC = 1.f / (QS_X1 * QS_WUP);
; #pragma unroll
;         for (int ai = 0; ai < 2; ++ai)
; #pragma unroll
;             for (int m = 0; m < 4; ++m) { unsigned char* rowp = H + (size_t)(row0 + ai * 128 + m * 16) * DM + col0; u32x2 w;
; #pragma unroll
;                 for (int n = 0; n < 2; ++n) { const f32x4 g = acc[ai][0][m][n] * SC + bgv[n], l = acc[ai][1][m][n] * SC + blv[n];
;                     const f32x2 o0 = act2((f32x2){g[0], g[1]}, (f32x2){l[0], l[1]}), o1 = act2((f32x2){g[2], g[3]}, (f32x2){l[2], l[3]});
;                     int r = 0; r = __builtin_amdgcn_cvt_pk_fp8_f32(e2m3q<EMU_DOWN != 0>(o0.x), e2m3q<EMU_DOWN != 0>(o0.y), r, false); r = __builtin_amdgcn_cvt_pk_fp8_f32(e2m3q<EMU_DOWN != 0>(o1.x), e2m3q<EMU_DOWN != 0>(o1.y), r, true);
;                     if (n == 0) w.x = (unsigned)r; else w.y = (unsigned)r; }
;                 *(u32x2*)rowp = w; }
	v_med3_f32 v23, v23, s47, v190
	v_med3_f32 v22, v22, s47, v190
	v_pk_fma_f32 v[22:23], v[22:23], 4.0, 4.0 op_sel_hi:[1,0,0]
	v_pk_add_f32 v[172:173], v[172:173], 1.0 op_sel_hi:[1,0]
	v_pk_fma_f32 v[174:175], v[40:41], s[36:37], v[4:5] op_sel_hi:[1,0,1]
	v_rcp_f32_e32 v172, v172
	v_rcp_f32_e32 v173, v173
	v_med3_f32 v175, v175, s47, v190
	v_med3_f32 v174, v174, s47, v190
	v_pk_fma_f32 v[174:175], v[174:175], 4.0, 4.0 op_sel_hi:[1,0,0]
	v_pk_mul_f32 v[18:19], v[18:19], v[172:173]
	v_pk_fma_f32 v[172:173], v[42:43], s[36:37], v[6:7] op_sel_hi:[1,0,1]
	v_pk_mul_f32 v[18:19], v[22:23], v[18:19]
	v_cvt_pk_fp8_f32 v150, v20, v21
	v_pk_fma_f32 v[20:21], v[72:73], s[36:37], v[0:1] op_sel_hi:[1,0,1]
	v_min_f32_e32 v21, 0x40e00000, v21
	v_min_f32_e32 v20, 0x40e00000, v20
	v_pk_mul_f32 v[176:177], v[20:21], s[78:79] op_sel_hi:[1,0]
	v_cvt_pk_fp8_f32 v150, v18, v19 op_sel:[0,0,1]
	v_exp_f32_e32 v176, v176
	v_exp_f32_e32 v177, v177
	v_pk_fma_f32 v[18:19], v[74:75], s[36:37], v[2:3] op_sel_hi:[1,0,1]
	v_med3_f32 v173, v173, s47, v190
	v_min_f32_e32 v19, 0x40e00000, v19
	v_pk_add_f32 v[176:177], v[176:177], 1.0 op_sel_hi:[1,0]
	v_min_f32_e32 v18, 0x40e00000, v18
	v_rcp_f32_e32 v176, v176
	v_rcp_f32_e32 v177, v177
	v_med3_f32 v172, v172, s47, v190
	v_pk_fma_f32 v[172:173], v[172:173], 4.0, 4.0 op_sel_hi:[1,0,0]
	s_mov_b32 s20, 0x24000
	v_pk_mul_f32 v[20:21], v[20:21], v[176:177]
	s_nop 0
	v_pk_mul_f32 v[20:21], v[174:175], v[20:21]
	v_pk_mul_f32 v[174:175], v[18:19], s[78:79] op_sel_hi:[1,0]
	v_cvt_pk_fp8_f32 v151, v20, v21
	v_exp_f32_e32 v174, v174
	v_exp_f32_e32 v175, v175
	v_pk_fma_f32 v[20:21], v[68:69], s[36:37], v[8:9] op_sel_hi:[1,0,1]
	v_pk_fma_f32 v[8:9], v[60:61], s[36:37], v[8:9] op_sel_hi:[1,0,1]
	v_min_f32_e32 v21, 0x40e00000, v21
	v_pk_add_f32 v[174:175], v[174:175], 1.0 op_sel_hi:[1,0]
	v_min_f32_e32 v20, 0x40e00000, v20
	v_rcp_f32_e32 v174, v174
	v_rcp_f32_e32 v175, v175
	v_min_f32_e32 v9, 0x40e00000, v9
	v_min_f32_e32 v8, 0x40e00000, v8
	v_pk_mul_f32 v[18:19], v[18:19], v[174:175]
	v_pk_mul_f32 v[174:175], v[20:21], s[78:79] op_sel_hi:[1,0]
	v_pk_mul_f32 v[18:19], v[172:173], v[18:19]
	v_exp_f32_e32 v174, v174
	v_exp_f32_e32 v175, v175
	v_cvt_pk_fp8_f32 v151, v18, v19 op_sel:[0,0,1]
	v_add_co_u32_e32 v18, vcc, s20, v16
	v_pk_add_f32 v[174:175], v[174:175], 1.0 op_sel_hi:[1,0]
	s_nop 0
	v_addc_co_u32_e32 v19, vcc, 0, v17, vcc
	v_rcp_f32_e32 v174, v174
	v_rcp_f32_e32 v175, v175
	v_pk_fma_f32 v[172:173], v[36:37], s[36:37], v[12:13] op_sel_hi:[1,0,1]
	v_permlane16_swap_b32_e32 v148, v150
	v_permlane16_swap_b32_e32 v149, v151
	global_store_dwordx4 v[146:147], v[148:151], off
	v_pk_fma_f32 v[18:19], v[70:71], s[36:37], v[10:11] op_sel_hi:[1,0,1]
	v_med3_f32 v173, v173, s47, v190
	v_med3_f32 v172, v172, s47, v190
	v_pk_mul_f32 v[20:21], v[20:21], v[174:175]
	v_pk_fma_f32 v[172:173], v[172:173], 4.0, 4.0 op_sel_hi:[1,0,0]
	v_min_f32_e32 v19, 0x40e00000, v19
	v_min_f32_e32 v18, 0x40e00000, v18
	v_pk_mul_f32 v[20:21], v[172:173], v[20:21]
	v_pk_mul_f32 v[172:173], v[18:19], s[78:79] op_sel_hi:[1,0]
	v_pk_fma_f32 v[22:23], v[38:39], s[36:37], v[14:15] op_sel_hi:[1,0,1]
	v_exp_f32_e32 v172, v172
	v_exp_f32_e32 v173, v173
	v_med3_f32 v23, v23, s47, v190
	v_med3_f32 v22, v22, s47, v190
	v_pk_fma_f32 v[22:23], v[22:23], 4.0, 4.0 op_sel_hi:[1,0,0]
	v_pk_add_f32 v[172:173], v[172:173], 1.0 op_sel_hi:[1,0]
	v_pk_fma_f32 v[174:175], v[32:33], s[36:37], v[4:5] op_sel_hi:[1,0,1]
	v_rcp_f32_e32 v172, v172
	v_rcp_f32_e32 v173, v173
	v_med3_f32 v175, v175, s47, v190
	v_med3_f32 v174, v174, s47, v190
	v_pk_fma_f32 v[174:175], v[174:175], 4.0, 4.0 op_sel_hi:[1,0,0]
	v_pk_mul_f32 v[18:19], v[18:19], v[172:173]
	v_pk_fma_f32 v[172:173], v[34:35], s[36:37], v[6:7] op_sel_hi:[1,0,1]
	v_pk_mul_f32 v[18:19], v[22:23], v[18:19]
	v_cvt_pk_fp8_f32 v148, v20, v21
	v_pk_fma_f32 v[20:21], v[64:65], s[36:37], v[0:1] op_sel_hi:[1,0,1]
	v_min_f32_e32 v21, 0x40e00000, v21
	v_min_f32_e32 v20, 0x40e00000, v20
	v_pk_mul_f32 v[176:177], v[20:21], s[78:79] op_sel_hi:[1,0]
; #define LAS __attribute__((address_space(3)))
; template <bool EMU> __device__ __forceinline__ float e2m3q(float y) { if constexpr (EMU) { y = fminf(fmaxf(y, -7.5f), 7.5f); return fabsf(y) < 1.f ? rintf(y * 8.f) * 0.125f : y; } else return y; }
;     static __device__ __forceinline__ f32x2 act2(f32x2 g, f32x2 l) {
;         g = __builtin_elementwise_min(g, (f32x2){7.f, 7.f}); l = __builtin_elementwise_min(__builtin_elementwise_max(l, (f32x2){-7.f, -7.f}), (f32x2){7.f, 7.f});
;         const f32x2 t = g * (-1.702f * 1.44269504089f); f32x2 e; e.x = __builtin_amdgcn_exp2f(t.x); e.y = __builtin_amdgcn_exp2f(t.y);
;         const f32x2 d = e + 1.0f; f32x2 r; r.x = __builtin_amdgcn_rcpf(d.x); r.y = __builtin_amdgcn_rcpf(d.y);
;         return (g * r) * (l * QS_ACT + QS_ACT);
;     }
;     __device__ __forceinline__ void operator()(const f32x4 (&acc)[2][2][4][2], const UnitD& u, int wr, int wc, int fr, int fq) const {
;         const int row0 = u.r0 + wr * 64 + fr, col0 = u.c0 + wc * 32 + 8 * fq;
;         const LAS float* bg = bl_lds + u.ui * 256 + wc * 32 + 8 * fq; const LAS float* bl = bg + 128;
;         f32x4 bgv[2], blv[2];
; #pragma unroll
;         for (int n = 0; n < 2; ++n) { bgv[n] = *(const LAS f32x4*)(bg + 4 * n); blv[n] = *(const LAS f32x4*)(bl + 4 * n); }
;         constexpr float SC = 1.f / (QS_X1 * QS_WUP);
; #pragma unroll
;         for (int ai = 0; ai < 2; ++ai)
; #pragma unroll
;             for (int m = 0; m < 4; ++m) { unsigned char* rowp = H + (size_t)(row0 + ai * 128 + m * 16) * DM + col0; u32x2 w;
; #pragma unroll
;                 for (int n = 0; n < 2; ++n) { const f32x4 g = acc[ai][0][m][n] * SC + bgv[n], l = acc[ai][1][m][n] * SC + blv[n];
;                     const f32x2 o0 = act2((f32x2){g[0], g[1]}, (f32x2){l[0], l[1]}), o1 = act2((f32x2){g[2], g[3]}, (f32x2){l[2], l[3]});
;                     int r = 0; r = __builtin_amdgcn_cvt_pk_fp8_f32(e2m3q<EMU_DOWN != 0>(o0.x), e2m3q<EMU_DOWN != 0>(o0.y), r, false); r = __builtin_amdgcn_cvt_pk_fp8_f32(e2m3q<EMU_DOWN != 0>(o1.x), e2m3q<EMU_DOWN != 0>(o1.y), r, true);
;                     if (n == 0) w.x = (unsigned)r; else w.y = (unsigned)r; }
;                 *(u32x2*)rowp = w; }
	v_cvt_pk_fp8_f32 v148, v18, v19 op_sel:[0,0,1]
	v_exp_f32_e32 v176, v176
	v_exp_f32_e32 v177, v177
	v_pk_fma_f32 v[18:19], v[66:67], s[36:37], v[2:3] op_sel_hi:[1,0,1]
	v_med3_f32 v173, v173, s47, v190
	v_min_f32_e32 v19, 0x40e00000, v19
	v_pk_add_f32 v[176:177], v[176:177], 1.0 op_sel_hi:[1,0]
	v_min_f32_e32 v18, 0x40e00000, v18
	v_rcp_f32_e32 v176, v176
	v_rcp_f32_e32 v177, v177
	v_med3_f32 v172, v172, s47, v190
	v_pk_fma_f32 v[172:173], v[172:173], 4.0, 4.0 op_sel_hi:[1,0,0]
	s_mov_b32 s20, 0x28000
	v_pk_mul_f32 v[20:21], v[20:21], v[176:177]
	v_pk_fma_f32 v[12:13], v[28:29], s[36:37], v[12:13] op_sel_hi:[1,0,1]
	v_pk_mul_f32 v[20:21], v[174:175], v[20:21]
	v_pk_mul_f32 v[174:175], v[18:19], s[78:79] op_sel_hi:[1,0]
	v_cvt_pk_fp8_f32 v149, v20, v21
	v_exp_f32_e32 v174, v174
	v_exp_f32_e32 v175, v175
	v_pk_fma_f32 v[10:11], v[62:63], s[36:37], v[10:11] op_sel_hi:[1,0,1]
	v_med3_f32 v13, v13, s47, v190
	v_med3_f32 v12, v12, s47, v190
	v_pk_add_f32 v[174:175], v[174:175], 1.0 op_sel_hi:[1,0]
	v_pk_fma_f32 v[14:15], v[30:31], s[36:37], v[14:15] op_sel_hi:[1,0,1]
	v_rcp_f32_e32 v174, v174
	v_rcp_f32_e32 v175, v175
	v_pk_fma_f32 v[12:13], v[12:13], 4.0, 4.0 op_sel_hi:[1,0,0]
	v_min_f32_e32 v11, 0x40e00000, v11
	v_min_f32_e32 v10, 0x40e00000, v10
	v_pk_mul_f32 v[18:19], v[18:19], v[174:175]
	v_pk_fma_f32 v[0:1], v[56:57], s[36:37], v[0:1] op_sel_hi:[1,0,1]
	v_pk_mul_f32 v[18:19], v[172:173], v[18:19]
	v_min_f32_e32 v1, 0x40e00000, v1
	v_cvt_pk_fp8_f32 v149, v18, v19 op_sel:[0,0,1]
	v_add_co_u32_e32 v18, vcc, s20, v16
	v_min_f32_e32 v0, 0x40e00000, v0
	s_nop 0
	v_addc_co_u32_e32 v19, vcc, 0, v17, vcc
	v_lshl_add_u64 v[146:147], v[18:19], 0, v[152:153]
	v_pk_mul_f32 v[18:19], v[8:9], s[78:79] op_sel_hi:[1,0]
	v_pk_fma_f32 v[4:5], v[24:25], s[36:37], v[4:5] op_sel_hi:[1,0,1]
	v_exp_f32_e32 v18, v18
	v_exp_f32_e32 v19, v19
	v_pk_fma_f32 v[2:3], v[58:59], s[36:37], v[2:3] op_sel_hi:[1,0,1]
	v_med3_f32 v5, v5, s47, v190
	v_med3_f32 v4, v4, s47, v190
	v_pk_add_f32 v[18:19], v[18:19], 1.0 op_sel_hi:[1,0]
	v_pk_fma_f32 v[6:7], v[26:27], s[36:37], v[6:7] op_sel_hi:[1,0,1]
	v_rcp_f32_e32 v18, v18
	v_rcp_f32_e32 v19, v19
	v_pk_fma_f32 v[4:5], v[4:5], 4.0, 4.0 op_sel_hi:[1,0,0]
	v_min_f32_e32 v3, 0x40e00000, v3
	v_min_f32_e32 v2, 0x40e00000, v2
	v_pk_mul_f32 v[8:9], v[8:9], v[18:19]
	s_nop 0
	v_pk_mul_f32 v[8:9], v[12:13], v[8:9]
	v_med3_f32 v13, v15, s47, v190
	v_med3_f32 v12, v14, s47, v190
	v_pk_mul_f32 v[14:15], v[10:11], s[78:79] op_sel_hi:[1,0]
	v_pk_fma_f32 v[12:13], v[12:13], 4.0, 4.0 op_sel_hi:[1,0,0]
	v_exp_f32_e32 v14, v14
	v_exp_f32_e32 v15, v15
	s_nop 0
	v_pk_add_f32 v[14:15], v[14:15], 1.0 op_sel_hi:[1,0]
	s_nop 0
	v_rcp_f32_e32 v14, v14
	v_rcp_f32_e32 v15, v15
	s_nop 0
	v_pk_mul_f32 v[10:11], v[10:11], v[14:15]
	s_nop 0
	v_pk_mul_f32 v[10:11], v[12:13], v[10:11]
	v_cvt_pk_fp8_f32 v150, v8, v9
	v_pk_mul_f32 v[8:9], v[0:1], s[78:79] op_sel_hi:[1,0]
	v_exp_f32_e32 v8, v8
	v_exp_f32_e32 v9, v9
	v_cvt_pk_fp8_f32 v150, v10, v11 op_sel:[0,0,1]
	v_pk_add_f32 v[8:9], v[8:9], 1.0 op_sel_hi:[1,0]
	s_nop 0
	v_rcp_f32_e32 v8, v8
	v_rcp_f32_e32 v9, v9
	s_nop 0
	v_pk_mul_f32 v[0:1], v[0:1], v[8:9]
	s_nop 0
	v_pk_mul_f32 v[0:1], v[4:5], v[0:1]
	v_med3_f32 v5, v7, s47, v190
	v_med3_f32 v4, v6, s47, v190
	v_pk_mul_f32 v[6:7], v[2:3], s[78:79] op_sel_hi:[1,0]
	v_cvt_pk_fp8_f32 v151, v0, v1
	v_exp_f32_e32 v6, v6
	v_exp_f32_e32 v7, v7
	v_pk_fma_f32 v[4:5], v[4:5], 4.0, 4.0 op_sel_hi:[1,0,0]
	v_add_co_u32_e32 v0, vcc, 0x2c000, v16
	v_pk_add_f32 v[6:7], v[6:7], 1.0 op_sel_hi:[1,0]
	s_nop 0
	v_addc_co_u32_e32 v1, vcc, 0, v17, vcc
	v_rcp_f32_e32 v6, v6
	v_rcp_f32_e32 v7, v7
	s_andn2_b64 vcc, exec, s[16:17]
	v_pk_mul_f32 v[2:3], v[2:3], v[6:7]
	s_nop 0
	v_pk_mul_f32 v[2:3], v[4:5], v[2:3]
	s_nop 0
	v_cvt_pk_fp8_f32 v151, v2, v3 op_sel:[0,0,1]
	s_nop 1
	v_permlane16_swap_b32_e32 v148, v150
	v_permlane16_swap_b32_e32 v149, v151
	global_store_dwordx4 v[146:147], v[148:151], off
	s_cbranch_vccnz .LBB0_759
	s_andn2_b64 vcc, exec, s[4:5]
	s_mov_b32 s86, 0x2f9636c4
	s_cbranch_vccnz .LBB0_758
	s_barrier

; #define LAS __attribute__((address_space(3)))
;     __device__ __forceinline__ void operator()(const f32x4 (&acc)[2][2][4][2], const UnitD& u, int wr, int wc, int fr, int fq) const {
;         const int row0 = u.r0 + wr * 64 + fr, col0 = u.c0 + wc * 32 + 8 * fq;
;         const LAS float* bias = bl_lds + u.ui * 256 + wc * 32 + 8 * fq;
; #pragma unroll
;         for (int bj = 0; bj < 2; ++bj) { const f32x4 bv0 = *(const LAS f32x4*)(bias + bj * 128) * QS_YS, bv1 = *(const LAS f32x4*)(bias + bj * 128 + 4) * QS_YS;
; #pragma unroll
;             for (int ai = 0; ai < 2; ++ai)
; #pragma unroll
;                 for (int m = 0; m < 4; ++m) { unsigned char* rowp = Y + (size_t)(row0 + ai * 128 + m * 16) * DM + col0 + bj * 128;
;                     const f32x4 v0 = acc[ai][bj][m][0] * (QS_YS / (QS_ACT * QS_WDOWN)) + bv0, v1 = acc[ai][bj][m][1] * (QS_YS / (QS_ACT * QS_WDOWN)) + bv1;
;                     u32x2 w; w.x = pk4_fp8(v0[0], v0[1], v0[2], v0[3]); w.y = pk4_fp8(v1[0], v1[1], v1[2], v1[3]);
;                     *(u32x2*)rowp = w; } }
;     }
.LBB0_872:
	v_bfe_u32 v152, v136, 4, 1
	v_mov_b32_e32 v128, v136
	v_mul_u32_u24_e32 v152, 0x3ff8, v152
	s_mov_b64 s[16:17], 0x4000
	v_and_b32_e32 v129, 15, v128
	v_ashrrev_i32_e32 v134, 2, v128
	v_lshrrev_b32_e32 v128, 1, v128
	v_and_b32_e32 v130, 0x60, v128
	v_and_b32_e32 v128, 24, v128
	v_add3_u32 v148, v130, s14, v128
	s_lshl_b32 s14, s64, 10
	s_add_i32 s14, s14, 0
	s_add_i32 s14, s14, 0x23100
	v_lshlrev_b32_e32 v130, 2, v130
	v_lshlrev_b32_e32 v128, 2, v128
	v_add3_u32 v143, s14, v130, v128
	ds_read_b128 v[130:133], v143
	ds_read_b128 v[144:147], v143 offset:16
	v_and_or_b32 v128, v134, s39, v129
	v_add_u32_e32 v150, s59, v128
	v_ashrrev_i32_e32 v151, 31, v150
	s_waitcnt lgkmcnt(0)
	v_pk_mul_f32 v[130:131], v[130:131], s[80:81] op_sel_hi:[1,0]
	v_pk_mul_f32 v[134:135], v[144:145], s[80:81] op_sel_hi:[1,0]
	v_pk_fma_f32 v[124:125], v[124:125], s[82:83], v[130:131] op_sel_hi:[1,0,1]
	v_pk_fma_f32 v[120:121], v[120:121], s[82:83], v[134:135] op_sel_hi:[1,0,1]
	v_med3_f32 v144, v124, s51, v187
	v_med3_f32 v125, v125, s51, v187
	v_cvt_pk_fp8_f32 v208, v144, v125
	v_med3_f32 v120, v120, s51, v187
	v_med3_f32 v121, v121, s51, v187
	v_cvt_pk_fp8_f32 v209, v120, v121
	v_pk_mul_f32 v[128:129], v[132:133], s[80:81] op_sel_hi:[1,0]
	v_pk_mul_f32 v[132:133], v[146:147], s[80:81] op_sel_hi:[1,0]
	v_pk_fma_f32 v[126:127], v[126:127], s[82:83], v[128:129] op_sel_hi:[1,0,1]
	v_pk_fma_f32 v[122:123], v[122:123], s[82:83], v[132:133] op_sel_hi:[1,0,1]
	v_med3_f32 v126, v126, s51, v187
	v_med3_f32 v127, v127, s51, v187
	v_med3_f32 v120, v122, s51, v187
	v_med3_f32 v121, v123, s51, v187
	v_cvt_pk_fp8_f32 v208, v126, v127 op_sel:[0,0,1]
	v_cvt_pk_fp8_f32 v209, v120, v121 op_sel:[0,0,1]
	v_lshlrev_b64 v[120:121], 10, v[150:151]
	v_ashrrev_i32_e32 v149, 31, v148
	v_lshl_add_u64 v[120:121], s[2:3], 0, v[120:121]
	v_lshl_add_u64 v[120:121], v[120:121], 0, v[148:149]
	v_pk_fma_f32 v[116:117], v[116:117], s[82:83], v[130:131] op_sel_hi:[1,0,1]
	v_pk_fma_f32 v[112:113], v[112:113], s[82:83], v[134:135] op_sel_hi:[1,0,1]
	v_med3_f32 v124, v116, s51, v187
	v_med3_f32 v117, v117, s51, v187
	v_pk_fma_f32 v[114:115], v[114:115], s[82:83], v[132:133] op_sel_hi:[1,0,1]
	v_cvt_pk_fp8_f32 v210, v124, v117
	v_med3_f32 v112, v112, s51, v187
	v_med3_f32 v113, v113, s51, v187
	v_pk_fma_f32 v[108:109], v[108:109], s[82:83], v[130:131] op_sel_hi:[1,0,1]
	v_cvt_pk_fp8_f32 v211, v112, v113
	v_med3_f32 v112, v114, s51, v187
	v_pk_fma_f32 v[104:105], v[104:105], s[82:83], v[134:135] op_sel_hi:[1,0,1]
	v_med3_f32 v114, v108, s51, v187
	v_med3_f32 v109, v109, s51, v187
	v_pk_fma_f32 v[106:107], v[106:107], s[82:83], v[132:133] op_sel_hi:[1,0,1]
	v_cvt_pk_fp8_f32 v212, v114, v109
	v_med3_f32 v104, v104, s51, v187
	v_med3_f32 v105, v105, s51, v187
	v_pk_fma_f32 v[100:101], v[100:101], s[82:83], v[130:131] op_sel_hi:[1,0,1]
	v_cvt_pk_fp8_f32 v213, v104, v105
	v_med3_f32 v104, v106, s51, v187
	v_pk_fma_f32 v[96:97], v[96:97], s[82:83], v[134:135] op_sel_hi:[1,0,1]
	v_med3_f32 v106, v100, s51, v187
	v_med3_f32 v101, v101, s51, v187
	v_pk_fma_f32 v[98:99], v[98:99], s[82:83], v[132:133] op_sel_hi:[1,0,1]
	v_cvt_pk_fp8_f32 v214, v106, v101
	v_med3_f32 v96, v96, s51, v187
	v_med3_f32 v97, v97, s51, v187
	v_pk_fma_f32 v[92:93], v[92:93], s[82:83], v[130:131] op_sel_hi:[1,0,1]
	v_cvt_pk_fp8_f32 v215, v96, v97
	v_med3_f32 v96, v98, s51, v187
	v_pk_fma_f32 v[88:89], v[88:89], s[82:83], v[134:135] op_sel_hi:[1,0,1]
	v_med3_f32 v98, v92, s51, v187
	v_med3_f32 v93, v93, s51, v187
	v_med3_f32 v113, v115, s51, v187
	s_movk_i32 s14, 0x4000
	v_pk_fma_f32 v[90:91], v[90:91], s[82:83], v[132:133] op_sel_hi:[1,0,1]
	v_cvt_pk_fp8_f32 v216, v98, v93
	v_med3_f32 v88, v88, s51, v187
	v_med3_f32 v89, v89, s51, v187
	v_pk_fma_f32 v[84:85], v[84:85], s[82:83], v[130:131] op_sel_hi:[1,0,1]
	v_cvt_pk_fp8_f32 v211, v112, v113 op_sel:[0,0,1]
	v_add_co_u32_e32 v112, vcc, s14, v120
	v_cvt_pk_fp8_f32 v217, v88, v89
	v_med3_f32 v88, v90, s51, v187
	v_pk_fma_f32 v[80:81], v[80:81], s[82:83], v[134:135] op_sel_hi:[1,0,1]
	v_med3_f32 v90, v84, s51, v187
	v_med3_f32 v85, v85, s51, v187
	v_addc_co_u32_e32 v113, vcc, 0, v121, vcc
	v_med3_f32 v105, v107, s51, v187
	s_mov_b32 s14, 0x8000
	v_pk_fma_f32 v[82:83], v[82:83], s[82:83], v[132:133] op_sel_hi:[1,0,1]
	v_cvt_pk_fp8_f32 v218, v90, v85
	v_med3_f32 v80, v80, s51, v187
	v_med3_f32 v81, v81, s51, v187
	v_pk_fma_f32 v[76:77], v[76:77], s[82:83], v[130:131] op_sel_hi:[1,0,1]
	v_cvt_pk_fp8_f32 v213, v104, v105 op_sel:[0,0,1]
	v_add_co_u32_e32 v104, vcc, s14, v120
	v_cvt_pk_fp8_f32 v219, v80, v81
	v_med3_f32 v80, v82, s51, v187
	v_pk_fma_f32 v[72:73], v[72:73], s[82:83], v[134:135] op_sel_hi:[1,0,1]
	v_med3_f32 v82, v76, s51, v187
	v_med3_f32 v77, v77, s51, v187
	v_addc_co_u32_e32 v105, vcc, 0, v121, vcc
	v_med3_f32 v97, v99, s51, v187
	s_mov_b32 s14, 0xc000
	v_cvt_pk_fp8_f32 v220, v82, v77
	v_med3_f32 v72, v72, s51, v187
	v_med3_f32 v73, v73, s51, v187
	v_cvt_pk_fp8_f32 v215, v96, v97 op_sel:[0,0,1]
	v_add_co_u32_e32 v96, vcc, s14, v120
	v_cvt_pk_fp8_f32 v221, v72, v73
	s_nop 0
	v_addc_co_u32_e32 v97, vcc, 0, v121, vcc
	v_med3_f32 v89, v91, s51, v187
	s_mov_b32 s14, 0x20000
	v_pk_fma_f32 v[118:119], v[118:119], s[82:83], v[128:129] op_sel_hi:[1,0,1]
	v_pk_fma_f32 v[110:111], v[110:111], s[82:83], v[128:129] op_sel_hi:[1,0,1]
	v_pk_fma_f32 v[102:103], v[102:103], s[82:83], v[128:129] op_sel_hi:[1,0,1]
	v_pk_fma_f32 v[94:95], v[94:95], s[82:83], v[128:129] op_sel_hi:[1,0,1]
	v_cvt_pk_fp8_f32 v217, v88, v89 op_sel:[0,0,1]
	v_add_co_u32_e32 v88, vcc, s14, v120
	v_pk_fma_f32 v[86:87], v[86:87], s[82:83], v[128:129] op_sel_hi:[1,0,1]
	v_pk_fma_f32 v[78:79], v[78:79], s[82:83], v[128:129] op_sel_hi:[1,0,1]
; #define LAS __attribute__((address_space(3)))
;     __device__ __forceinline__ void operator()(const f32x4 (&acc)[2][2][4][2], const UnitD& u, int wr, int wc, int fr, int fq) const {
;         const int row0 = u.r0 + wr * 64 + fr, col0 = u.c0 + wc * 32 + 8 * fq;
;         const LAS float* bias = bl_lds + u.ui * 256 + wc * 32 + 8 * fq;
; #pragma unroll
;         for (int bj = 0; bj < 2; ++bj) { const f32x4 bv0 = *(const LAS f32x4*)(bias + bj * 128) * QS_YS, bv1 = *(const LAS f32x4*)(bias + bj * 128 + 4) * QS_YS;
; #pragma unroll
;             for (int ai = 0; ai < 2; ++ai)
; #pragma unroll
;                 for (int m = 0; m < 4; ++m) { unsigned char* rowp = Y + (size_t)(row0 + ai * 128 + m * 16) * DM + col0 + bj * 128;
;                     const f32x4 v0 = acc[ai][bj][m][0] * (QS_YS / (QS_ACT * QS_WDOWN)) + bv0, v1 = acc[ai][bj][m][1] * (QS_YS / (QS_ACT * QS_WDOWN)) + bv1;
;                     u32x2 w; w.x = pk4_fp8(v0[0], v0[1], v0[2], v0[3]); w.y = pk4_fp8(v1[0], v1[1], v1[2], v1[3]);
;                     *(u32x2*)rowp = w; } }
;     }
	v_pk_fma_f32 v[74:75], v[74:75], s[82:83], v[132:133] op_sel_hi:[1,0,1]
	v_med3_f32 v118, v118, s51, v187
	v_med3_f32 v119, v119, s51, v187
	v_med3_f32 v110, v110, s51, v187
	v_med3_f32 v111, v111, s51, v187
	v_med3_f32 v102, v102, s51, v187
	v_med3_f32 v103, v103, s51, v187
	v_med3_f32 v94, v94, s51, v187
	v_med3_f32 v95, v95, s51, v187
	v_addc_co_u32_e32 v89, vcc, 0, v121, vcc
	v_med3_f32 v86, v86, s51, v187
	v_med3_f32 v87, v87, s51, v187
	v_med3_f32 v81, v83, s51, v187
	s_mov_b32 s14, 0x24000
	v_med3_f32 v78, v78, s51, v187
	v_med3_f32 v79, v79, s51, v187
	v_med3_f32 v72, v74, s51, v187
	v_med3_f32 v73, v75, s51, v187
	v_pk_fma_f32 v[68:69], v[68:69], s[82:83], v[130:131] op_sel_hi:[1,0,1]
	v_pk_fma_f32 v[64:65], v[64:65], s[82:83], v[134:135] op_sel_hi:[1,0,1]
	v_cvt_pk_fp8_f32 v210, v118, v119 op_sel:[0,0,1]
	v_cvt_pk_fp8_f32 v212, v110, v111 op_sel:[0,0,1]
	v_cvt_pk_fp8_f32 v214, v102, v103 op_sel:[0,0,1]
	v_cvt_pk_fp8_f32 v216, v94, v95 op_sel:[0,0,1]
	v_cvt_pk_fp8_f32 v218, v86, v87 op_sel:[0,0,1]
	v_cvt_pk_fp8_f32 v219, v80, v81 op_sel:[0,0,1]
	v_add_co_u32_e32 v80, vcc, s14, v120
	v_cvt_pk_fp8_f32 v220, v78, v79 op_sel:[0,0,1]
	v_cvt_pk_fp8_f32 v221, v72, v73 op_sel:[0,0,1]
	v_med3_f32 v68, v68, s51, v187
	v_med3_f32 v69, v69, s51, v187
	v_med3_f32 v64, v64, s51, v187
	v_med3_f32 v65, v65, s51, v187
	v_addc_co_u32_e32 v81, vcc, 0, v121, vcc
	s_mov_b32 s14, 0x28000
	v_cvt_pk_fp8_f32 v222, v68, v69
	v_cvt_pk_fp8_f32 v223, v64, v65
	v_add_co_u32_e32 v72, vcc, s14, v120
	v_pk_fma_f32 v[70:71], v[70:71], s[82:83], v[128:129] op_sel_hi:[1,0,1]
	s_nop 0
	v_addc_co_u32_e32 v73, vcc, 0, v121, vcc
	v_pk_fma_f32 v[66:67], v[66:67], s[82:83], v[132:133] op_sel_hi:[1,0,1]
	v_permlane16_swap_b32_e32 v208, v210
	v_permlane16_swap_b32_e32 v209, v211
	v_permlane16_swap_b32_e32 v212, v214
	v_permlane16_swap_b32_e32 v213, v215
	v_permlane16_swap_b32_e32 v216, v218
	v_permlane16_swap_b32_e32 v217, v219
	v_lshl_add_u64 v[224:225], v[120:121], 0, v[152:153]
	v_lshl_add_u64 v[226:227], v[104:105], 0, v[152:153]
	v_lshl_add_u64 v[228:229], v[88:89], 0, v[152:153]
	v_lshl_add_u64 v[230:231], v[72:73], 0, v[152:153]
	global_store_dwordx4 v[224:225], v[208:211], off
	global_store_dwordx4 v[226:227], v[212:215], off
	global_store_dwordx4 v[228:229], v[216:219], off
	v_med3_f32 v70, v70, s51, v187
	v_med3_f32 v71, v71, s51, v187
	v_med3_f32 v64, v66, s51, v187
	v_med3_f32 v65, v67, s51, v187
	v_cvt_pk_fp8_f32 v222, v70, v71 op_sel:[0,0,1]
	v_cvt_pk_fp8_f32 v223, v64, v65 op_sel:[0,0,1]
	ds_read_b128 v[64:67], v143 offset:512
	ds_read_b128 v[68:71], v143 offset:528
	s_mov_b32 s14, 0x2c000
	s_waitcnt lgkmcnt(0)
	v_pk_mul_f32 v[64:65], v[64:65], s[80:81] op_sel_hi:[1,0]
	v_pk_mul_f32 v[68:69], v[68:69], s[80:81] op_sel_hi:[1,0]
	v_pk_fma_f32 v[60:61], v[60:61], s[82:83], v[64:65] op_sel_hi:[1,0,1]
	v_pk_fma_f32 v[56:57], v[56:57], s[82:83], v[68:69] op_sel_hi:[1,0,1]
	v_permlane16_swap_b32_e32 v220, v222
	v_permlane16_swap_b32_e32 v221, v223
	global_store_dwordx4 v[230:231], v[220:223], off
	v_med3_f32 v74, v60, s51, v187
	v_med3_f32 v61, v61, s51, v187
	v_cvt_pk_fp8_f32 v192, v74, v61
	v_med3_f32 v56, v56, s51, v187
	v_med3_f32 v57, v57, s51, v187
	v_cvt_pk_fp8_f32 v193, v56, v57
	v_pk_mul_f32 v[70:71], v[70:71], s[80:81] op_sel_hi:[1,0]
	v_pk_fma_f32 v[52:53], v[52:53], s[82:83], v[64:65] op_sel_hi:[1,0,1]
	v_pk_fma_f32 v[58:59], v[58:59], s[82:83], v[70:71] op_sel_hi:[1,0,1]
	v_pk_fma_f32 v[48:49], v[48:49], s[82:83], v[68:69] op_sel_hi:[1,0,1]
	v_med3_f32 v56, v58, s51, v187
	v_med3_f32 v57, v59, s51, v187
	v_cvt_pk_fp8_f32 v193, v56, v57 op_sel:[0,0,1]
	v_med3_f32 v56, v52, s51, v187
	v_med3_f32 v53, v53, s51, v187
	v_cvt_pk_fp8_f32 v194, v56, v53
	v_med3_f32 v48, v48, s51, v187
	v_med3_f32 v49, v49, s51, v187
	v_cvt_pk_fp8_f32 v195, v48, v49
	v_pk_fma_f32 v[50:51], v[50:51], s[82:83], v[70:71] op_sel_hi:[1,0,1]
	v_pk_fma_f32 v[44:45], v[44:45], s[82:83], v[64:65] op_sel_hi:[1,0,1]
	v_med3_f32 v48, v50, s51, v187
	v_med3_f32 v49, v51, s51, v187
	v_cvt_pk_fp8_f32 v195, v48, v49 op_sel:[0,0,1]
	v_pk_fma_f32 v[40:41], v[40:41], s[82:83], v[68:69] op_sel_hi:[1,0,1]
	v_med3_f32 v48, v44, s51, v187
	v_med3_f32 v45, v45, s51, v187
	v_cvt_pk_fp8_f32 v196, v48, v45
	v_med3_f32 v40, v40, s51, v187
	v_med3_f32 v41, v41, s51, v187
	v_cvt_pk_fp8_f32 v197, v40, v41
	v_pk_fma_f32 v[42:43], v[42:43], s[82:83], v[70:71] op_sel_hi:[1,0,1]
	v_pk_fma_f32 v[36:37], v[36:37], s[82:83], v[64:65] op_sel_hi:[1,0,1]
	v_med3_f32 v40, v42, s51, v187
	v_med3_f32 v41, v43, s51, v187
	v_cvt_pk_fp8_f32 v197, v40, v41 op_sel:[0,0,1]
	v_pk_fma_f32 v[32:33], v[32:33], s[82:83], v[68:69] op_sel_hi:[1,0,1]
	v_med3_f32 v40, v36, s51, v187
	v_med3_f32 v37, v37, s51, v187
	v_cvt_pk_fp8_f32 v198, v40, v37
	v_med3_f32 v32, v32, s51, v187
	v_med3_f32 v33, v33, s51, v187
	v_cvt_pk_fp8_f32 v199, v32, v33
	v_pk_fma_f32 v[34:35], v[34:35], s[82:83], v[70:71] op_sel_hi:[1,0,1]
	v_pk_fma_f32 v[28:29], v[28:29], s[82:83], v[64:65] op_sel_hi:[1,0,1]
; #define LAS __attribute__((address_space(3)))
;     __device__ __forceinline__ void operator()(const f32x4 (&acc)[2][2][4][2], const UnitD& u, int wr, int wc, int fr, int fq) const {
;         const int row0 = u.r0 + wr * 64 + fr, col0 = u.c0 + wc * 32 + 8 * fq;
;         const LAS float* bias = bl_lds + u.ui * 256 + wc * 32 + 8 * fq;
; #pragma unroll
;         for (int bj = 0; bj < 2; ++bj) { const f32x4 bv0 = *(const LAS f32x4*)(bias + bj * 128) * QS_YS, bv1 = *(const LAS f32x4*)(bias + bj * 128 + 4) * QS_YS;
; #pragma unroll
;             for (int ai = 0; ai < 2; ++ai)
; #pragma unroll
;                 for (int m = 0; m < 4; ++m) { unsigned char* rowp = Y + (size_t)(row0 + ai * 128 + m * 16) * DM + col0 + bj * 128;
;                     const f32x4 v0 = acc[ai][bj][m][0] * (QS_YS / (QS_ACT * QS_WDOWN)) + bv0, v1 = acc[ai][bj][m][1] * (QS_YS / (QS_ACT * QS_WDOWN)) + bv1;
;                     u32x2 w; w.x = pk4_fp8(v0[0], v0[1], v0[2], v0[3]); w.y = pk4_fp8(v1[0], v1[1], v1[2], v1[3]);
;                     *(u32x2*)rowp = w; } }
;     }
	v_med3_f32 v32, v34, s51, v187
	v_med3_f32 v33, v35, s51, v187
	v_cvt_pk_fp8_f32 v199, v32, v33 op_sel:[0,0,1]
	v_pk_fma_f32 v[24:25], v[24:25], s[82:83], v[68:69] op_sel_hi:[1,0,1]
	v_med3_f32 v32, v28, s51, v187
	v_med3_f32 v29, v29, s51, v187
	v_cvt_pk_fp8_f32 v200, v32, v29
	v_med3_f32 v24, v24, s51, v187
	v_med3_f32 v25, v25, s51, v187
	v_cvt_pk_fp8_f32 v201, v24, v25
	v_pk_fma_f32 v[26:27], v[26:27], s[82:83], v[70:71] op_sel_hi:[1,0,1]
	v_pk_fma_f32 v[20:21], v[20:21], s[82:83], v[64:65] op_sel_hi:[1,0,1]
	v_med3_f32 v24, v26, s51, v187
	v_med3_f32 v25, v27, s51, v187
	v_cvt_pk_fp8_f32 v201, v24, v25 op_sel:[0,0,1]
	v_pk_fma_f32 v[16:17], v[16:17], s[82:83], v[68:69] op_sel_hi:[1,0,1]
	v_med3_f32 v24, v20, s51, v187
	v_med3_f32 v21, v21, s51, v187
	v_cvt_pk_fp8_f32 v202, v24, v21
	v_med3_f32 v16, v16, s51, v187
	v_med3_f32 v17, v17, s51, v187
	v_cvt_pk_fp8_f32 v203, v16, v17
	v_pk_fma_f32 v[18:19], v[18:19], s[82:83], v[70:71] op_sel_hi:[1,0,1]
	v_pk_fma_f32 v[12:13], v[12:13], s[82:83], v[64:65] op_sel_hi:[1,0,1]
	v_med3_f32 v16, v18, s51, v187
	v_med3_f32 v17, v19, s51, v187
	v_cvt_pk_fp8_f32 v203, v16, v17 op_sel:[0,0,1]
	v_pk_fma_f32 v[8:9], v[8:9], s[82:83], v[68:69] op_sel_hi:[1,0,1]
	v_med3_f32 v16, v12, s51, v187
	v_med3_f32 v13, v13, s51, v187
	v_cvt_pk_fp8_f32 v204, v16, v13
	v_med3_f32 v8, v8, s51, v187
	v_med3_f32 v9, v9, s51, v187
	v_cvt_pk_fp8_f32 v205, v8, v9
	v_pk_fma_f32 v[10:11], v[10:11], s[82:83], v[70:71] op_sel_hi:[1,0,1]
	v_pk_fma_f32 v[4:5], v[4:5], s[82:83], v[64:65] op_sel_hi:[1,0,1]
	v_med3_f32 v8, v10, s51, v187
	v_med3_f32 v9, v11, s51, v187
	v_pk_mul_f32 v[66:67], v[66:67], s[80:81] op_sel_hi:[1,0]
	v_cvt_pk_fp8_f32 v205, v8, v9 op_sel:[0,0,1]
	v_pk_fma_f32 v[0:1], v[0:1], s[82:83], v[68:69] op_sel_hi:[1,0,1]
	v_med3_f32 v8, v4, s51, v187
	v_med3_f32 v5, v5, s51, v187
	v_pk_fma_f32 v[62:63], v[62:63], s[82:83], v[66:67] op_sel_hi:[1,0,1]
	v_pk_fma_f32 v[30:31], v[30:31], s[82:83], v[66:67] op_sel_hi:[1,0,1]
	v_cvt_pk_fp8_f32 v206, v8, v5
	v_med3_f32 v0, v0, s51, v187
	v_med3_f32 v1, v1, s51, v187
	v_lshl_add_u64 v[122:123], v[120:121], 0, s[16:17]
	s_mov_b64 s[16:17], 0xc000
	v_med3_f32 v62, v62, s51, v187
	v_med3_f32 v63, v63, s51, v187
	v_pk_fma_f32 v[54:55], v[54:55], s[82:83], v[66:67] op_sel_hi:[1,0,1]
	v_med3_f32 v30, v30, s51, v187
	v_med3_f32 v31, v31, s51, v187
	v_pk_fma_f32 v[22:23], v[22:23], s[82:83], v[66:67] op_sel_hi:[1,0,1]
	v_cvt_pk_fp8_f32 v207, v0, v1
	v_lshl_add_u64 v[104:105], v[120:121], 0, s[16:17]
	s_mov_b64 s[16:17], 0x20000
	v_cvt_pk_fp8_f32 v192, v62, v63 op_sel:[0,0,1]
	v_med3_f32 v54, v54, s51, v187
	v_med3_f32 v55, v55, s51, v187
	v_pk_fma_f32 v[46:47], v[46:47], s[82:83], v[66:67] op_sel_hi:[1,0,1]
	v_cvt_pk_fp8_f32 v200, v30, v31 op_sel:[0,0,1]
	v_med3_f32 v22, v22, s51, v187
	v_med3_f32 v23, v23, s51, v187
	v_pk_fma_f32 v[14:15], v[14:15], s[82:83], v[66:67] op_sel_hi:[1,0,1]
	v_lshl_add_u64 v[96:97], v[120:121], 0, s[16:17]
	s_mov_b64 s[16:17], 0x24000
	v_cvt_pk_fp8_f32 v194, v54, v55 op_sel:[0,0,1]
	v_med3_f32 v46, v46, s51, v187
	v_med3_f32 v47, v47, s51, v187
	v_pk_fma_f32 v[38:39], v[38:39], s[82:83], v[66:67] op_sel_hi:[1,0,1]
	v_cvt_pk_fp8_f32 v202, v22, v23 op_sel:[0,0,1]
	v_med3_f32 v14, v14, s51, v187
	v_med3_f32 v15, v15, s51, v187
	v_pk_fma_f32 v[6:7], v[6:7], s[82:83], v[66:67] op_sel_hi:[1,0,1]
	v_pk_fma_f32 v[2:3], v[2:3], s[82:83], v[70:71] op_sel_hi:[1,0,1]
	v_lshl_add_u64 v[88:89], v[120:121], 0, s[16:17]
	s_mov_b64 s[16:17], 0x28000
	v_cvt_pk_fp8_f32 v196, v46, v47 op_sel:[0,0,1]
	v_med3_f32 v38, v38, s51, v187
	v_med3_f32 v39, v39, s51, v187
	v_cvt_pk_fp8_f32 v204, v14, v15 op_sel:[0,0,1]
	v_med3_f32 v6, v6, s51, v187
	v_med3_f32 v7, v7, s51, v187
	v_med3_f32 v0, v2, s51, v187
	v_med3_f32 v1, v3, s51, v187
	v_lshl_add_u64 v[80:81], v[120:121], 0, s[16:17]
	s_mov_b64 s[16:17], 0x2c000
	v_cvt_pk_fp8_f32 v198, v38, v39 op_sel:[0,0,1]
	v_cvt_pk_fp8_f32 v206, v6, v7 op_sel:[0,0,1]
	v_cvt_pk_fp8_f32 v207, v0, v1 op_sel:[0,0,1]
	s_andn2_b64 vcc, exec, s[12:13]
	s_mov_b64 s[12:13], -1
	v_lshl_add_u64 v[112:113], v[120:121], 0, s[60:61]
	v_permlane16_swap_b32_e32 v192, v194
	v_permlane16_swap_b32_e32 v193, v195
	v_permlane16_swap_b32_e32 v196, v198
	v_permlane16_swap_b32_e32 v197, v199
	v_permlane16_swap_b32_e32 v200, v202
	v_permlane16_swap_b32_e32 v201, v203
	v_lshl_add_u64 v[232:233], v[120:121], 0, v[152:153]
	v_lshl_add_u64 v[234:235], v[112:113], 0, v[152:153]
	v_permlane16_swap_b32_e32 v204, v206
	v_permlane16_swap_b32_e32 v205, v207
	v_lshl_add_u64 v[236:237], v[96:97], 0, v[152:153]
	v_lshl_add_u64 v[238:239], v[80:81], 0, v[152:153]
	global_store_dwordx4 v[232:233], v[192:195], off offset:128
	global_store_dwordx4 v[234:235], v[196:199], off offset:128
	global_store_dwordx4 v[236:237], v[200:203], off offset:128
	global_store_dwordx4 v[238:239], v[204:207], off offset:128
	s_cbranch_vccnz .LBB0_853
	s_andn2_b64 vcc, exec, s[0:1]
	s_cbranch_vccnz .LBB0_852
	s_barrier
	s_branch .LBB0_852
